# PLE gate epilogue: -log2e of the sigmoid folded into pre-scaled row scales and biases (98 fewer multiplies per unit epilogue)
# baseline (speedup 1.0000x reference)
; __device__ __forceinline__ float fsigmoid(float x) { return __builtin_amdgcn_rcpf(1.f + __builtin_amdgcn_exp2f(-x * LOG2E)); }
; __device__ __forceinline__ float fgelu(float x) { const float y = 1.5957691216057308f * (x + 0.044715f * x * x * x); return x * __builtin_amdgcn_rcpf(1.f + __builtin_amdgcn_exp2f(-y * LOG2E)); }
; __device__ __forceinline__ unsigned cvt_pk_bf16(float lo, float hi) { return pk2(lo, hi); }
;     __device__ __forceinline__ void operator()(const f32x4 (&acc)[2][2][4][2], const Unit& u, int wr, int wc, int fr, int fq) const {
;     ...
; #pragma unroll
;         for (int ai = 0; ai < 2; ++ai)
; #pragma unroll
;             for (int m = 0; m < 4; ++m) rsv[ai][m] = rs ? rs[row0 + ai * HALF + m * 16] : 1.f;
;         f32x4 bv[2][2];
; #pragma unroll
;         for (int bj = 0; bj < 2; ++bj)
; #pragma unroll
;             for (int n = 0; n < 2; ++n) bv[bj][n] = bs ? *(const f32x4*)(bs + col0 + bj * HALF + 4 * n) : (f32x4){0.f, 0.f, 0.f, 0.f};
; #pragma unroll
;         for (int ai = 0; ai < 2; ++ai)
; #pragma unroll
;             for (int m = 0; m < 4; ++m) { bf16_t* rowp = base + (size_t)(row0 + ai * HALF + m * 16) * ldc + col0; const float sc = rsv[ai][m];
; #pragma unroll
;                 for (int bj = 0; bj < 2; ++bj) { f32x4 v0 = acc[ai][bj][m][0], v1 = acc[ai][bj][m][1];
;                     if (rs) { v0 *= sc; v1 *= sc; }
;                     v0 += bv[bj][0]; v1 += bv[bj][1];
;                     if (ACT == 1) { for (int e = 0; e < 4; ++e) { v0[e] = fgelu(v0[e]); v1[e] = fgelu(v1[e]); } }
;                     if (ACT == 2) { for (int e = 0; e < 4; ++e) { v0[e] = fsigmoid(v0[e]); v1[e] = fsigmoid(v1[e]); } }
;                     u32x4 w; w.x = cvt_pk_bf16(v0[0], v0[1]); w.y = cvt_pk_bf16(v0[2], v0[3]); w.z = cvt_pk_bf16(v1[0], v1[1]); w.w = cvt_pk_bf16(v1[2], v1[3]);
;                     *(u32x4*)(rowp + bj * HALF) = w; } }
.LBB0_1184:
	s_waitcnt vmcnt(0)
	v_mul_f32_e32 v162, 0xbfb8aa3b, v162
	v_mul_f32_e32 v166, 0xbfb8aa3b, v166
	v_mul_f32_e32 v168, 0xbfb8aa3b, v168
	v_mul_f32_e32 v170, 0xbfb8aa3b, v170
	v_mul_f32_e32 v172, 0xbfb8aa3b, v172
	v_mul_f32_e32 v180, 0xbfb8aa3b, v180
	v_mul_f32_e32 v182, 0xbfb8aa3b, v182
	v_mul_f32_e32 v184, 0xbfb8aa3b, v184
	v_mul_f32_e32 v106, 0xbfb8aa3b, v106
	v_mul_f32_e32 v107, 0xbfb8aa3b, v107
	v_mul_f32_e32 v108, 0xbfb8aa3b, v108
	v_mul_f32_e32 v109, 0xbfb8aa3b, v109
	v_mul_f32_e32 v110, 0xbfb8aa3b, v110
	v_mul_f32_e32 v111, 0xbfb8aa3b, v111
	v_mul_f32_e32 v112, 0xbfb8aa3b, v112
	v_mul_f32_e32 v113, 0xbfb8aa3b, v113
	v_mul_f32_e32 v114, 0xbfb8aa3b, v114
	v_mul_f32_e32 v115, 0xbfb8aa3b, v115
	v_mul_f32_e32 v116, 0xbfb8aa3b, v116
	v_mul_f32_e32 v117, 0xbfb8aa3b, v117
	v_mul_f32_e32 v118, 0xbfb8aa3b, v118
	v_mul_f32_e32 v119, 0xbfb8aa3b, v119
	v_mul_f32_e32 v120, 0xbfb8aa3b, v120
	v_mul_f32_e32 v121, 0xbfb8aa3b, v121
	v_pk_fma_f32 v[138:139], v[138:139], v[184:185], v[114:115] op_sel_hi:[1,0,1]
	v_pk_fma_f32 v[142:143], v[142:143], v[184:185], v[118:119] op_sel_hi:[1,0,1]
	s_nop 0
	v_exp_f32_e32 v138, v138
	s_nop 0
	v_exp_f32_e32 v143, v143
	v_pk_fma_f32 v[144:145], v[144:145], v[184:185], v[120:121] op_sel_hi:[1,0,1]
	v_add_f32_e32 v138, 1.0, v138
	s_nop 0
	v_exp_f32_e32 v139, v139
	v_rcp_f32_e32 v171, v138
	v_add_f32_e32 v138, 1.0, v143
	v_mov_b32_e32 v143, v144
	v_exp_f32_e32 v143, v143
	v_pk_fma_f32 v[140:141], v[140:141], v[184:185], v[116:117] op_sel_hi:[1,0,1]
	v_add_f32_e32 v139, 1.0, v139
	s_nop 0
	s_nop 0
	v_exp_f32_e32 v140, v140
	v_rcp_f32_e32 v144, v139
	v_add_f32_e32 v139, 1.0, v143
	v_mov_b32_e32 v143, v145
	s_nop 0
	v_exp_f32_e32 v142, v142
	v_exp_f32_e32 v143, v143
	v_exp_f32_e32 v141, v141
	v_add_f32_e32 v140, 1.0, v140
	v_pk_fma_f32 v[130:131], v[130:131], v[184:185], v[106:107] op_sel_hi:[1,0,1]
	v_add_f32_e32 v142, 1.0, v142
	v_rcp_f32_e32 v145, v140
	v_add_f32_e32 v140, 1.0, v143
	v_add_f32_e32 v141, 1.0, v141
	v_pk_fma_f32 v[134:135], v[134:135], v[184:185], v[110:111] op_sel_hi:[1,0,1]
	s_nop 0
	v_rcp_f32_e32 v142, v142
	v_rcp_f32_e32 v138, v138
	v_rcp_f32_e32 v139, v139
	v_rcp_f32_e32 v140, v140
	v_rcp_f32_e32 v141, v141
	v_exp_f32_e32 v130, v130
	s_nop 0
	v_exp_f32_e32 v135, v135
	v_lshl_add_u64 v[176:177], v[164:165], 1, s[8:9]
	v_lshlrev_b64 v[164:165], 11, v[178:179]
	v_lshl_add_u64 v[164:165], v[176:177], 0, v[164:165]
	v_cvt_pk_bf16_f32 v138, v142, v138
	v_cvt_pk_bf16_f32 v139, v139, v140
	v_cvt_pk_bf16_f32 v140, v171, v144
	v_cvt_pk_bf16_f32 v141, v145, v141
	v_pk_fma_f32 v[136:137], v[136:137], v[184:185], v[112:113] op_sel_hi:[1,0,1]
	v_add_f32_e32 v130, 1.0, v130
	s_nop 0
	global_store_dwordx4 v[164:165], v[138:141], off
	v_exp_f32_e32 v131, v131
	v_pk_fma_f32 v[132:133], v[132:133], v[184:185], v[108:109] op_sel_hi:[1,0,1]
	v_rcp_f32_e32 v138, v130
	v_add_f32_e32 v130, 1.0, v135
	v_mov_b32_e32 v135, v136
	v_exp_f32_e32 v135, v135
	v_add_f32_e32 v131, 1.0, v131
	s_nop 0
	s_nop 0
	v_exp_f32_e32 v132, v132
	v_rcp_f32_e32 v136, v131
	v_add_f32_e32 v131, 1.0, v135
	v_mov_b32_e32 v135, v137
	s_nop 0
	v_exp_f32_e32 v134, v134
	v_exp_f32_e32 v135, v135
	v_exp_f32_e32 v133, v133
	v_add_f32_e32 v132, 1.0, v132
	v_pk_fma_f32 v[122:123], v[122:123], v[182:183], v[114:115] op_sel_hi:[1,0,1]
	v_add_f32_e32 v134, 1.0, v134
	v_rcp_f32_e32 v137, v132
	v_add_f32_e32 v132, 1.0, v135
	v_add_f32_e32 v133, 1.0, v133
	v_pk_fma_f32 v[126:127], v[126:127], v[182:183], v[118:119] op_sel_hi:[1,0,1]
	s_nop 0
	v_rcp_f32_e32 v134, v134
	v_rcp_f32_e32 v130, v130
	v_rcp_f32_e32 v131, v131
	v_rcp_f32_e32 v132, v132
	v_rcp_f32_e32 v133, v133
	v_exp_f32_e32 v122, v122
	s_nop 0
	v_exp_f32_e32 v127, v127
	v_cvt_pk_bf16_f32 v130, v134, v130
	v_cvt_pk_bf16_f32 v131, v131, v132
	v_cvt_pk_bf16_f32 v132, v138, v136
	v_cvt_pk_bf16_f32 v133, v137, v133
	v_pk_fma_f32 v[128:129], v[128:129], v[182:183], v[120:121] op_sel_hi:[1,0,1]
	v_add_f32_e32 v122, 1.0, v122
	s_nop 0
	global_store_dwordx4 v[164:165], v[130:133], off offset:256
	v_exp_f32_e32 v123, v123
	v_pk_fma_f32 v[124:125], v[124:125], v[182:183], v[116:117] op_sel_hi:[1,0,1]
	v_rcp_f32_e32 v132, v122
	v_add_f32_e32 v122, 1.0, v127
	v_mov_b32_e32 v127, v128
	v_exp_f32_e32 v127, v127
	v_add_f32_e32 v123, 1.0, v123
	s_nop 0
	s_nop 0
	v_exp_f32_e32 v124, v124
	v_rcp_f32_e32 v128, v123
	v_add_f32_e32 v123, 1.0, v127
	v_mov_b32_e32 v127, v129
	s_nop 0
	v_exp_f32_e32 v126, v126
	v_exp_f32_e32 v127, v127
	v_exp_f32_e32 v125, v125
	v_add_f32_e32 v124, 1.0, v124
	v_pk_fma_f32 v[98:99], v[98:99], v[182:183], v[106:107] op_sel_hi:[1,0,1]
	v_add_f32_e32 v126, 1.0, v126
	v_rcp_f32_e32 v129, v124
	v_add_f32_e32 v124, 1.0, v127
	v_add_f32_e32 v125, 1.0, v125
	v_pk_fma_f32 v[102:103], v[102:103], v[182:183], v[110:111] op_sel_hi:[1,0,1]
	s_nop 0
	v_rcp_f32_e32 v126, v126
	v_rcp_f32_e32 v122, v122
	v_rcp_f32_e32 v123, v123
	v_rcp_f32_e32 v124, v124
	v_rcp_f32_e32 v125, v125
	v_exp_f32_e32 v98, v98
	s_nop 0
	v_or_b32_e32 v130, 16, v178
	v_exp_f32_e32 v103, v103
	v_ashrrev_i32_e32 v131, 31, v130
	v_lshlrev_b64 v[130:131], 11, v[130:131]
	v_lshl_add_u64 v[130:131], v[176:177], 0, v[130:131]
	v_cvt_pk_bf16_f32 v122, v126, v122
	v_cvt_pk_bf16_f32 v123, v123, v124
	v_cvt_pk_bf16_f32 v124, v132, v128
	v_cvt_pk_bf16_f32 v125, v129, v125
	v_pk_fma_f32 v[104:105], v[104:105], v[182:183], v[112:113] op_sel_hi:[1,0,1]
	v_add_f32_e32 v98, 1.0, v98
	s_nop 0
	global_store_dwordx4 v[130:131], v[122:125], off
	v_exp_f32_e32 v99, v99
	v_pk_fma_f32 v[100:101], v[100:101], v[182:183], v[108:109] op_sel_hi:[1,0,1]
	v_rcp_f32_e32 v122, v98
	v_add_f32_e32 v98, 1.0, v103
	v_mov_b32_e32 v103, v104
	v_exp_f32_e32 v103, v103
; __device__ __forceinline__ float fsigmoid(float x) { return __builtin_amdgcn_rcpf(1.f + __builtin_amdgcn_exp2f(-x * LOG2E)); }
; __device__ __forceinline__ float fgelu(float x) { const float y = 1.5957691216057308f * (x + 0.044715f * x * x * x); return x * __builtin_amdgcn_rcpf(1.f + __builtin_amdgcn_exp2f(-y * LOG2E)); }
; __device__ __forceinline__ unsigned cvt_pk_bf16(float lo, float hi) { return pk2(lo, hi); }
;     __device__ __forceinline__ void operator()(const f32x4 (&acc)[2][2][4][2], const Unit& u, int wr, int wc, int fr, int fq) const {
;     ...
;         for (int ai = 0; ai < 2; ++ai)
; #pragma unroll
;             for (int m = 0; m < 4; ++m) { bf16_t* rowp = base + (size_t)(row0 + ai * HALF + m * 16) * ldc + col0; const float sc = rsv[ai][m];
; #pragma unroll
;                 for (int bj = 0; bj < 2; ++bj) { f32x4 v0 = acc[ai][bj][m][0], v1 = acc[ai][bj][m][1];
;                     if (rs) { v0 *= sc; v1 *= sc; }
;                     v0 += bv[bj][0]; v1 += bv[bj][1];
;                     if (ACT == 1) { for (int e = 0; e < 4; ++e) { v0[e] = fgelu(v0[e]); v1[e] = fgelu(v1[e]); } }
;                     if (ACT == 2) { for (int e = 0; e < 4; ++e) { v0[e] = fsigmoid(v0[e]); v1[e] = fsigmoid(v1[e]); } }
;                     u32x4 w; w.x = cvt_pk_bf16(v0[0], v0[1]); w.y = cvt_pk_bf16(v0[2], v0[3]); w.z = cvt_pk_bf16(v1[0], v1[1]); w.w = cvt_pk_bf16(v1[2], v1[3]);
;                     *(u32x4*)(rowp + bj * HALF) = w; } }
	v_add_f32_e32 v99, 1.0, v99
	s_nop 0
	s_nop 0
	v_exp_f32_e32 v100, v100
	v_rcp_f32_e32 v104, v99
	v_add_f32_e32 v99, 1.0, v103
	v_mov_b32_e32 v103, v105
	s_nop 0
	v_exp_f32_e32 v102, v102
	v_exp_f32_e32 v103, v103
	v_exp_f32_e32 v101, v101
	v_add_f32_e32 v100, 1.0, v100
	v_pk_fma_f32 v[90:91], v[90:91], v[180:181], v[114:115] op_sel_hi:[1,0,1]
	v_add_f32_e32 v102, 1.0, v102
	v_rcp_f32_e32 v105, v100
	v_add_f32_e32 v100, 1.0, v103
	v_add_f32_e32 v101, 1.0, v101
	v_pk_fma_f32 v[94:95], v[94:95], v[180:181], v[118:119] op_sel_hi:[1,0,1]
	s_nop 0
	v_rcp_f32_e32 v102, v102
	v_rcp_f32_e32 v98, v98
	v_rcp_f32_e32 v99, v99
	v_rcp_f32_e32 v100, v100
	v_rcp_f32_e32 v101, v101
	v_exp_f32_e32 v90, v90
	s_nop 0
	v_exp_f32_e32 v95, v95
	v_cvt_pk_bf16_f32 v98, v102, v98
	v_cvt_pk_bf16_f32 v99, v99, v100
	v_cvt_pk_bf16_f32 v100, v122, v104
	v_cvt_pk_bf16_f32 v101, v105, v101
	v_pk_fma_f32 v[96:97], v[96:97], v[180:181], v[120:121] op_sel_hi:[1,0,1]
	v_add_f32_e32 v90, 1.0, v90
	s_nop 0
	global_store_dwordx4 v[130:131], v[98:101], off offset:256
	v_exp_f32_e32 v91, v91
	v_pk_fma_f32 v[92:93], v[92:93], v[180:181], v[116:117] op_sel_hi:[1,0,1]
	v_rcp_f32_e32 v100, v90
	v_add_f32_e32 v90, 1.0, v95
	v_mov_b32_e32 v95, v96
	v_exp_f32_e32 v95, v95
	v_add_f32_e32 v91, 1.0, v91
	s_nop 0
	s_nop 0
	v_exp_f32_e32 v92, v92
	v_rcp_f32_e32 v96, v91
	v_add_f32_e32 v91, 1.0, v95
	v_mov_b32_e32 v95, v97
	s_nop 0
	v_exp_f32_e32 v94, v94
	v_exp_f32_e32 v95, v95
	v_exp_f32_e32 v93, v93
	v_add_f32_e32 v92, 1.0, v92
	v_pk_fma_f32 v[82:83], v[82:83], v[180:181], v[106:107] op_sel_hi:[1,0,1]
	v_add_f32_e32 v94, 1.0, v94
	v_rcp_f32_e32 v97, v92
	v_add_f32_e32 v92, 1.0, v95
	v_add_f32_e32 v93, 1.0, v93
	v_pk_fma_f32 v[86:87], v[86:87], v[180:181], v[110:111] op_sel_hi:[1,0,1]
	s_nop 0
	v_rcp_f32_e32 v94, v94
	v_rcp_f32_e32 v90, v90
	v_rcp_f32_e32 v91, v91
	v_rcp_f32_e32 v92, v92
	v_rcp_f32_e32 v93, v93
	v_exp_f32_e32 v82, v82
	s_nop 0
	v_or_b32_e32 v98, 32, v178
	v_exp_f32_e32 v87, v87
	v_ashrrev_i32_e32 v99, 31, v98
	v_lshlrev_b64 v[98:99], 11, v[98:99]
	v_lshl_add_u64 v[98:99], v[176:177], 0, v[98:99]
	v_cvt_pk_bf16_f32 v90, v94, v90
	v_cvt_pk_bf16_f32 v91, v91, v92
	v_cvt_pk_bf16_f32 v92, v100, v96
	v_cvt_pk_bf16_f32 v93, v97, v93
	v_pk_fma_f32 v[88:89], v[88:89], v[180:181], v[112:113] op_sel_hi:[1,0,1]
	v_add_f32_e32 v82, 1.0, v82
	s_nop 0
	global_store_dwordx4 v[98:99], v[90:93], off
	v_exp_f32_e32 v83, v83
	v_pk_fma_f32 v[84:85], v[84:85], v[180:181], v[108:109] op_sel_hi:[1,0,1]
	v_rcp_f32_e32 v90, v82
	v_add_f32_e32 v82, 1.0, v87
	v_mov_b32_e32 v87, v88
	v_exp_f32_e32 v87, v87
	v_add_f32_e32 v83, 1.0, v83
	s_nop 0
	s_nop 0
	v_exp_f32_e32 v84, v84
	v_rcp_f32_e32 v88, v83
	v_add_f32_e32 v83, 1.0, v87
	v_mov_b32_e32 v87, v89
	s_nop 0
	v_exp_f32_e32 v86, v86
	v_exp_f32_e32 v87, v87
	v_exp_f32_e32 v85, v85
	v_add_f32_e32 v84, 1.0, v84
	v_pk_fma_f32 v[74:75], v[74:75], v[172:173], v[114:115] op_sel_hi:[1,0,1]
	v_add_f32_e32 v86, 1.0, v86
	v_rcp_f32_e32 v89, v84
	v_add_f32_e32 v84, 1.0, v87
	v_add_f32_e32 v85, 1.0, v85
	v_pk_fma_f32 v[78:79], v[78:79], v[172:173], v[118:119] op_sel_hi:[1,0,1]
	s_nop 0
	v_rcp_f32_e32 v86, v86
	v_rcp_f32_e32 v82, v82
	v_rcp_f32_e32 v83, v83
	v_rcp_f32_e32 v84, v84
	v_rcp_f32_e32 v85, v85
	v_exp_f32_e32 v74, v74
	s_nop 0
	v_exp_f32_e32 v79, v79
	v_cvt_pk_bf16_f32 v82, v86, v82
	v_cvt_pk_bf16_f32 v83, v83, v84
	v_cvt_pk_bf16_f32 v84, v90, v88
	v_cvt_pk_bf16_f32 v85, v89, v85
	v_pk_fma_f32 v[80:81], v[80:81], v[172:173], v[120:121] op_sel_hi:[1,0,1]
	v_add_f32_e32 v74, 1.0, v74
	s_nop 0
	global_store_dwordx4 v[98:99], v[82:85], off offset:256
	v_exp_f32_e32 v75, v75
	v_pk_fma_f32 v[76:77], v[76:77], v[172:173], v[116:117] op_sel_hi:[1,0,1]
	v_rcp_f32_e32 v84, v74
	v_add_f32_e32 v74, 1.0, v79
	v_mov_b32_e32 v79, v80
	v_exp_f32_e32 v79, v79
	v_add_f32_e32 v75, 1.0, v75
	s_nop 0
	s_nop 0
	v_exp_f32_e32 v76, v76
	v_rcp_f32_e32 v80, v75
	v_add_f32_e32 v75, 1.0, v79
	v_mov_b32_e32 v79, v81
	s_nop 0
	v_exp_f32_e32 v78, v78
	v_exp_f32_e32 v79, v79
	v_exp_f32_e32 v77, v77
	v_add_f32_e32 v76, 1.0, v76
	v_pk_fma_f32 v[66:67], v[66:67], v[172:173], v[106:107] op_sel_hi:[1,0,1]
	v_add_f32_e32 v78, 1.0, v78
	v_rcp_f32_e32 v81, v76
	v_add_f32_e32 v76, 1.0, v79
	v_add_f32_e32 v77, 1.0, v77
	v_pk_fma_f32 v[70:71], v[70:71], v[172:173], v[110:111] op_sel_hi:[1,0,1]
	s_nop 0
	v_rcp_f32_e32 v78, v78
	v_rcp_f32_e32 v74, v74
	v_rcp_f32_e32 v75, v75
	v_rcp_f32_e32 v76, v76
	v_rcp_f32_e32 v77, v77
	s_nop 0
	v_exp_f32_e32 v66, v66
	s_nop 0
	v_or_b32_e32 v82, 48, v178
	v_exp_f32_e32 v70, v70
	v_exp_f32_e32 v71, v71
	v_ashrrev_i32_e32 v83, 31, v82
	v_lshlrev_b64 v[82:83], 11, v[82:83]
	v_pk_fma_f32 v[58:59], v[58:59], v[170:171], v[114:115] op_sel_hi:[1,0,1]
	v_lshl_add_u64 v[82:83], v[176:177], 0, v[82:83]
	v_cvt_pk_bf16_f32 v74, v78, v74
	v_cvt_pk_bf16_f32 v75, v75, v76
	v_cvt_pk_bf16_f32 v76, v84, v80
	v_cvt_pk_bf16_f32 v77, v81, v77
	v_add_f32_e32 v66, 1.0, v66
	v_pk_fma_f32 v[62:63], v[62:63], v[170:171], v[118:119] op_sel_hi:[1,0,1]
	s_nop 0
	global_store_dwordx4 v[82:83], v[74:77], off
	v_add_f32_e32 v70, 1.0, v70
	v_exp_f32_e32 v58, v58
	v_rcp_f32_e32 v74, v66
	v_add_f32_e32 v66, 1.0, v71
	s_nop 0
	v_pk_fma_f32 v[72:73], v[72:73], v[172:173], v[112:113] op_sel_hi:[1,0,1]
	v_rcp_f32_e32 v70, v70
	s_nop 0
	v_rcp_f32_e32 v66, v66
	v_exp_f32_e32 v63, v63
	v_exp_f32_e32 v67, v67
	v_mov_b32_e32 v71, v72
	v_exp_f32_e32 v71, v71
	v_pk_fma_f32 v[64:65], v[64:65], v[170:171], v[120:121] op_sel_hi:[1,0,1]
	v_add_f32_e32 v58, 1.0, v58
	s_nop 0
	v_pk_fma_f32 v[68:69], v[68:69], v[172:173], v[108:109] op_sel_hi:[1,0,1]
	v_cvt_pk_bf16_f32 v66, v70, v66
	v_exp_f32_e32 v59, v59
; __device__ __forceinline__ float fsigmoid(float x) { return __builtin_amdgcn_rcpf(1.f + __builtin_amdgcn_exp2f(-x * LOG2E)); }
; __device__ __forceinline__ float fgelu(float x) { const float y = 1.5957691216057308f * (x + 0.044715f * x * x * x); return x * __builtin_amdgcn_rcpf(1.f + __builtin_amdgcn_exp2f(-y * LOG2E)); }
; __device__ __forceinline__ unsigned cvt_pk_bf16(float lo, float hi) { return pk2(lo, hi); }
;     __device__ __forceinline__ void operator()(const f32x4 (&acc)[2][2][4][2], const Unit& u, int wr, int wc, int fr, int fq) const {
;     ...
;         for (int ai = 0; ai < 2; ++ai)
; #pragma unroll
;             for (int m = 0; m < 4; ++m) { bf16_t* rowp = base + (size_t)(row0 + ai * HALF + m * 16) * ldc + col0; const float sc = rsv[ai][m];
; #pragma unroll
;                 for (int bj = 0; bj < 2; ++bj) { f32x4 v0 = acc[ai][bj][m][0], v1 = acc[ai][bj][m][1];
;                     if (rs) { v0 *= sc; v1 *= sc; }
;                     v0 += bv[bj][0]; v1 += bv[bj][1];
;                     if (ACT == 1) { for (int e = 0; e < 4; ++e) { v0[e] = fgelu(v0[e]); v1[e] = fgelu(v1[e]); } }
;                     if (ACT == 2) { for (int e = 0; e < 4; ++e) { v0[e] = fsigmoid(v0[e]); v1[e] = fsigmoid(v1[e]); } }
;                     u32x4 w; w.x = cvt_pk_bf16(v0[0], v0[1]); w.y = cvt_pk_bf16(v0[2], v0[3]); w.z = cvt_pk_bf16(v1[0], v1[1]); w.w = cvt_pk_bf16(v1[2], v1[3]);
;                     *(u32x4*)(rowp + bj * HALF) = w; } }
	v_rcp_f32_e32 v70, v58
	v_add_f32_e32 v58, 1.0, v63
	v_mov_b32_e32 v63, v64
	v_add_f32_e32 v67, 1.0, v67
	s_nop 0
	v_exp_f32_e32 v63, v63
	v_exp_f32_e32 v68, v68
	v_rcp_f32_e32 v72, v67
	v_add_f32_e32 v67, 1.0, v71
	v_mov_b32_e32 v71, v73
	s_nop 0
	v_exp_f32_e32 v71, v71
	v_exp_f32_e32 v69, v69
	v_pk_fma_f32 v[60:61], v[60:61], v[170:171], v[116:117] op_sel_hi:[1,0,1]
	s_nop 0
	v_add_f32_e32 v59, 1.0, v59
	s_nop 0
	v_exp_f32_e32 v62, v62
	v_exp_f32_e32 v60, v60
	v_rcp_f32_e32 v64, v59
	v_add_f32_e32 v59, 1.0, v63
	v_mov_b32_e32 v63, v65
	s_nop 0
	v_add_f32_e32 v68, 1.0, v68
	v_exp_f32_e32 v63, v63
	v_exp_f32_e32 v61, v61
	v_rcp_f32_e32 v73, v68
	v_add_f32_e32 v68, 1.0, v71
	v_add_f32_e32 v69, 1.0, v69
	v_rcp_f32_e32 v67, v67
	v_rcp_f32_e32 v68, v68
	v_rcp_f32_e32 v69, v69
	v_add_f32_e32 v62, 1.0, v62
	v_add_f32_e32 v60, 1.0, v60
	v_pk_fma_f32 v[50:51], v[50:51], v[170:171], v[106:107] op_sel_hi:[1,0,1]
	v_rcp_f32_e32 v62, v62
	v_rcp_f32_e32 v58, v58
	v_rcp_f32_e32 v65, v60
	v_add_f32_e32 v60, 1.0, v63
	v_add_f32_e32 v61, 1.0, v61
	v_pk_fma_f32 v[54:55], v[54:55], v[170:171], v[110:111] op_sel_hi:[1,0,1]
	s_nop 0
	v_rcp_f32_e32 v59, v59
	v_rcp_f32_e32 v60, v60
	v_rcp_f32_e32 v61, v61
	v_exp_f32_e32 v50, v50
	s_nop 0
	v_lshlrev_b64 v[174:175], 11, v[178:179]
	v_cvt_pk_bf16_f32 v67, v67, v68
	v_cvt_pk_bf16_f32 v68, v74, v72
	v_cvt_pk_bf16_f32 v69, v73, v69
	v_exp_f32_e32 v55, v55
	global_store_dwordx4 v[82:83], v[66:69], off offset:256
	v_cvt_pk_bf16_f32 v58, v62, v58
	v_cvt_pk_bf16_f32 v59, v59, v60
	v_lshl_add_u64 v[66:67], v[176:177], 0, v[174:175]
	v_add_co_u32_e32 v62, vcc, s83, v66
	v_cvt_pk_bf16_f32 v60, v70, v64
	v_cvt_pk_bf16_f32 v61, v65, v61
	v_addc_co_u32_e32 v63, vcc, 0, v67, vcc
	v_pk_fma_f32 v[56:57], v[56:57], v[170:171], v[112:113] op_sel_hi:[1,0,1]
	v_add_f32_e32 v50, 1.0, v50
	s_nop 0
	global_store_dwordx4 v[62:63], v[58:61], off
	v_exp_f32_e32 v51, v51
	v_pk_fma_f32 v[52:53], v[52:53], v[170:171], v[108:109] op_sel_hi:[1,0,1]
	v_rcp_f32_e32 v58, v50
	v_add_f32_e32 v50, 1.0, v55
	v_mov_b32_e32 v55, v56
	v_exp_f32_e32 v55, v55
	v_add_f32_e32 v51, 1.0, v51
	s_nop 0
	s_nop 0
	v_exp_f32_e32 v52, v52
	v_rcp_f32_e32 v56, v51
	v_add_f32_e32 v51, 1.0, v55
	v_mov_b32_e32 v55, v57
	s_nop 0
	v_exp_f32_e32 v54, v54
	v_exp_f32_e32 v55, v55
	v_exp_f32_e32 v53, v53
	v_add_f32_e32 v52, 1.0, v52
	v_pk_fma_f32 v[42:43], v[42:43], v[168:169], v[114:115] op_sel_hi:[1,0,1]
	v_add_f32_e32 v54, 1.0, v54
	v_rcp_f32_e32 v57, v52
	v_add_f32_e32 v52, 1.0, v55
	v_add_f32_e32 v53, 1.0, v53
	v_pk_fma_f32 v[46:47], v[46:47], v[168:169], v[118:119] op_sel_hi:[1,0,1]
	s_nop 0
	v_rcp_f32_e32 v54, v54
	v_rcp_f32_e32 v50, v50
	v_rcp_f32_e32 v51, v51
	v_rcp_f32_e32 v52, v52
	v_rcp_f32_e32 v53, v53
	v_exp_f32_e32 v42, v42
	s_nop 0
	v_exp_f32_e32 v47, v47
	s_mov_b64 s[6:7], 0x40000
	v_lshl_add_u64 v[68:69], v[66:67], 0, s[6:7]
	v_cvt_pk_bf16_f32 v50, v54, v50
	v_cvt_pk_bf16_f32 v51, v51, v52
	v_cvt_pk_bf16_f32 v52, v58, v56
	v_cvt_pk_bf16_f32 v53, v57, v53
	v_pk_fma_f32 v[48:49], v[48:49], v[168:169], v[120:121] op_sel_hi:[1,0,1]
	v_add_f32_e32 v42, 1.0, v42
	s_nop 0
	global_store_dwordx4 v[68:69], v[50:53], off offset:256
	v_exp_f32_e32 v43, v43
	v_pk_fma_f32 v[44:45], v[44:45], v[168:169], v[116:117] op_sel_hi:[1,0,1]
	v_rcp_f32_e32 v52, v42
	v_add_f32_e32 v42, 1.0, v47
	v_mov_b32_e32 v47, v48
	v_exp_f32_e32 v47, v47
	s_nop 0
	v_add_f32_e32 v43, 1.0, v43
	s_nop 0
	v_exp_f32_e32 v46, v46
	v_exp_f32_e32 v44, v44
	v_rcp_f32_e32 v48, v43
	v_add_f32_e32 v43, 1.0, v47
	v_mov_b32_e32 v47, v49
	s_nop 0
	v_exp_f32_e32 v47, v47
	v_exp_f32_e32 v45, v45
	v_add_f32_e32 v46, 1.0, v46
	v_add_f32_e32 v44, 1.0, v44
	v_pk_fma_f32 v[34:35], v[34:35], v[168:169], v[106:107] op_sel_hi:[1,0,1]
	v_rcp_f32_e32 v46, v46
	v_rcp_f32_e32 v42, v42
	v_rcp_f32_e32 v49, v44
	v_add_f32_e32 v44, 1.0, v47
	v_add_f32_e32 v45, 1.0, v45
	v_pk_fma_f32 v[38:39], v[38:39], v[168:169], v[110:111] op_sel_hi:[1,0,1]
	s_nop 0
	v_rcp_f32_e32 v43, v43
	v_rcp_f32_e32 v44, v44
	v_rcp_f32_e32 v45, v45
	v_exp_f32_e32 v34, v34
	s_nop 0
	s_mov_b64 s[6:7], 0x48000
	v_exp_f32_e32 v39, v39
	v_lshl_add_u64 v[50:51], v[164:165], 0, s[6:7]
	s_mov_b32 s6, 0x48000
	v_cvt_pk_bf16_f32 v42, v46, v42
	v_add_co_u32_e32 v46, vcc, s6, v164
	v_cvt_pk_bf16_f32 v43, v43, v44
	v_cvt_pk_bf16_f32 v44, v52, v48
	v_cvt_pk_bf16_f32 v45, v49, v45
	v_addc_co_u32_e32 v47, vcc, 0, v165, vcc
	v_pk_fma_f32 v[40:41], v[40:41], v[168:169], v[112:113] op_sel_hi:[1,0,1]
	v_add_f32_e32 v34, 1.0, v34
	s_nop 0
	global_store_dwordx4 v[46:47], v[42:45], off
	v_exp_f32_e32 v35, v35
	v_pk_fma_f32 v[36:37], v[36:37], v[168:169], v[108:109] op_sel_hi:[1,0,1]
	v_rcp_f32_e32 v42, v34
	v_add_f32_e32 v34, 1.0, v39
	v_mov_b32_e32 v39, v40
	v_exp_f32_e32 v39, v39
	v_add_f32_e32 v35, 1.0, v35
	s_nop 0
	s_nop 0
	v_exp_f32_e32 v36, v36
	v_rcp_f32_e32 v40, v35
	v_add_f32_e32 v35, 1.0, v39
	v_mov_b32_e32 v39, v41
	s_nop 0
	v_exp_f32_e32 v38, v38
	v_exp_f32_e32 v39, v39
	v_exp_f32_e32 v37, v37
	v_add_f32_e32 v36, 1.0, v36
	v_pk_fma_f32 v[18:19], v[18:19], v[166:167], v[114:115] op_sel_hi:[1,0,1]
	v_add_f32_e32 v38, 1.0, v38
	v_rcp_f32_e32 v41, v36
	v_add_f32_e32 v36, 1.0, v39
	v_add_f32_e32 v37, 1.0, v37
	v_pk_fma_f32 v[22:23], v[22:23], v[166:167], v[118:119] op_sel_hi:[1,0,1]
	s_nop 0
; __device__ __forceinline__ float fsigmoid(float x) { return __builtin_amdgcn_rcpf(1.f + __builtin_amdgcn_exp2f(-x * LOG2E)); }
; __device__ __forceinline__ float fgelu(float x) { const float y = 1.5957691216057308f * (x + 0.044715f * x * x * x); return x * __builtin_amdgcn_rcpf(1.f + __builtin_amdgcn_exp2f(-y * LOG2E)); }
; __device__ __forceinline__ unsigned cvt_pk_bf16(float lo, float hi) { return pk2(lo, hi); }
; #define PG8_BAR __builtin_amdgcn_s_barrier()
; template <class Epi, class Sched>
; __device__ __forceinline__ void gemm_phase(PG8_LAS unsigned char* lds, const int K, const Sched& S, const Epi& E, const int wave_s) {
;     ...
;         cur = nxt; cA = nA; cB = nB; ++ui;
; #pragma unroll
;         for (int h = 0; h < 2; ++h)
; #pragma unroll
;             for (int i = 0; i < 2; ++i) vA[h][i] = vN[h][i];
;         if (wr == 1) PG8_BAR;
;     __device__ __forceinline__ void operator()(const f32x4 (&acc)[2][2][4][2], const Unit& u, int wr, int wc, int fr, int fq) const {
;     ...
;             for (int m = 0; m < 4; ++m) { bf16_t* rowp = base + (size_t)(row0 + ai * HALF + m * 16) * ldc + col0; const float sc = rsv[ai][m];
; #pragma unroll
;                 for (int bj = 0; bj < 2; ++bj) { f32x4 v0 = acc[ai][bj][m][0], v1 = acc[ai][bj][m][1];
;                     if (rs) { v0 *= sc; v1 *= sc; }
;                     v0 += bv[bj][0]; v1 += bv[bj][1];
;                     if (ACT == 1) { for (int e = 0; e < 4; ++e) { v0[e] = fgelu(v0[e]); v1[e] = fgelu(v1[e]); } }
;                     if (ACT == 2) { for (int e = 0; e < 4; ++e) { v0[e] = fsigmoid(v0[e]); v1[e] = fsigmoid(v1[e]); } }
;                     u32x4 w; w.x = cvt_pk_bf16(v0[0], v0[1]); w.y = cvt_pk_bf16(v0[2], v0[3]); w.z = cvt_pk_bf16(v1[0], v1[1]); w.w = cvt_pk_bf16(v1[2], v1[3]);
;                     *(u32x4*)(rowp + bj * HALF) = w; } }
	v_rcp_f32_e32 v38, v38
	v_rcp_f32_e32 v34, v34
	v_rcp_f32_e32 v35, v35
	v_rcp_f32_e32 v36, v36
	v_rcp_f32_e32 v37, v37
	v_exp_f32_e32 v18, v18
	s_nop 0
	v_exp_f32_e32 v23, v23
	v_cvt_pk_bf16_f32 v34, v38, v34
	v_cvt_pk_bf16_f32 v35, v35, v36
	v_cvt_pk_bf16_f32 v36, v42, v40
	v_cvt_pk_bf16_f32 v37, v41, v37
	v_pk_fma_f32 v[24:25], v[24:25], v[166:167], v[120:121] op_sel_hi:[1,0,1]
	v_add_f32_e32 v18, 1.0, v18
	s_nop 0
	global_store_dwordx4 v[50:51], v[34:37], off offset:256
	v_exp_f32_e32 v19, v19
	v_pk_fma_f32 v[20:21], v[20:21], v[166:167], v[116:117] op_sel_hi:[1,0,1]
	v_rcp_f32_e32 v36, v18
	v_add_f32_e32 v18, 1.0, v23
	v_mov_b32_e32 v23, v24
	v_exp_f32_e32 v23, v23
	s_nop 0
	v_add_f32_e32 v19, 1.0, v19
	s_nop 0
	v_exp_f32_e32 v22, v22
	v_exp_f32_e32 v20, v20
	v_rcp_f32_e32 v24, v19
	v_add_f32_e32 v19, 1.0, v23
	v_mov_b32_e32 v23, v25
	s_nop 0
	v_exp_f32_e32 v23, v23
	v_exp_f32_e32 v21, v21
	v_add_f32_e32 v22, 1.0, v22
	v_add_f32_e32 v20, 1.0, v20
	v_rcp_f32_e32 v22, v22
	v_rcp_f32_e32 v18, v18
	v_rcp_f32_e32 v25, v20
	v_add_f32_e32 v20, 1.0, v23
	v_add_f32_e32 v21, 1.0, v21
	v_rcp_f32_e32 v19, v19
	v_rcp_f32_e32 v20, v20
	v_rcp_f32_e32 v21, v21
	v_cvt_pk_bf16_f32 v18, v22, v18
	v_add_co_u32_e32 v22, vcc, s90, v164
	v_cvt_pk_bf16_f32 v19, v19, v20
	v_cvt_pk_bf16_f32 v20, v36, v24
	v_cvt_pk_bf16_f32 v21, v25, v21
	v_addc_co_u32_e32 v23, vcc, 0, v165, vcc
	global_store_dwordx4 v[22:23], v[18:21], off
	v_pk_fma_f32 v[24:25], v[28:29], v[166:167], v[108:109] op_sel_hi:[1,0,1]
	v_pk_fma_f32 v[22:23], v[26:27], v[166:167], v[106:107] op_sel_hi:[1,0,1]
	v_pk_fma_f32 v[18:19], v[32:33], v[166:167], v[112:113] op_sel_hi:[1,0,1]
	s_nop 0
	s_nop 0
	v_exp_f32_e32 v18, v18
	v_exp_f32_e32 v24, v24
	v_pk_fma_f32 v[20:21], v[30:31], v[166:167], v[110:111] op_sel_hi:[1,0,1]
	s_nop 0
	v_add_f32_e32 v18, 1.0, v18
	s_nop 0
	s_nop 0
	s_nop 0
	s_nop 0
	v_rcp_f32_e32 v26, v18
	v_add_f32_e32 v18, 1.0, v24
	v_exp_f32_e32 v19, v19
	v_mov_b32_e32 v24, v25
	v_exp_f32_e32 v20, v20
	v_exp_f32_e32 v22, v22
	v_exp_f32_e32 v21, v21
	v_exp_f32_e32 v23, v23
	v_exp_f32_e32 v24, v24
	v_rcp_f32_e32 v25, v18
	v_add_f32_e32 v18, 1.0, v19
	v_pk_fma_f32 v[2:3], v[2:3], v[162:163], v[114:115] op_sel_hi:[1,0,1]
	v_add_f32_e32 v20, 1.0, v20
	v_add_f32_e32 v22, 1.0, v22
	v_add_f32_e32 v21, 1.0, v21
	v_add_f32_e32 v23, 1.0, v23
	v_rcp_f32_e32 v19, v18
	v_add_f32_e32 v18, 1.0, v24
	v_pk_fma_f32 v[6:7], v[6:7], v[162:163], v[118:119] op_sel_hi:[1,0,1]
	s_nop 0
	v_rcp_f32_e32 v20, v20
	v_rcp_f32_e32 v22, v22
	v_rcp_f32_e32 v21, v21
	v_rcp_f32_e32 v23, v23
	v_rcp_f32_e32 v24, v18
	v_exp_f32_e32 v2, v2
	s_nop 0
	v_exp_f32_e32 v7, v7
	s_mov_b64 s[6:7], 0x50000
	v_lshl_add_u64 v[34:35], v[164:165], 0, s[6:7]
	v_cvt_pk_bf16_f32 v18, v20, v21
	v_cvt_pk_bf16_f32 v19, v26, v19
	v_cvt_pk_bf16_f32 v20, v22, v23
	v_cvt_pk_bf16_f32 v21, v25, v24
	v_pk_fma_f32 v[8:9], v[8:9], v[162:163], v[120:121] op_sel_hi:[1,0,1]
	v_add_f32_e32 v2, 1.0, v2
	s_nop 0
	global_store_dwordx4 v[34:35], v[18:21], off offset:256
	v_exp_f32_e32 v3, v3
	v_pk_fma_f32 v[4:5], v[4:5], v[162:163], v[116:117] op_sel_hi:[1,0,1]
	v_rcp_f32_e32 v20, v2
	v_add_f32_e32 v2, 1.0, v7
	v_mov_b32_e32 v7, v8
	v_exp_f32_e32 v7, v7
	s_nop 0
	v_add_f32_e32 v3, 1.0, v3
	s_nop 0
	v_exp_f32_e32 v6, v6
	v_exp_f32_e32 v4, v4
	v_rcp_f32_e32 v8, v3
	v_add_f32_e32 v3, 1.0, v7
	v_mov_b32_e32 v7, v9
	s_nop 0
	v_exp_f32_e32 v7, v7
	v_exp_f32_e32 v5, v5
	v_add_f32_e32 v6, 1.0, v6
	v_add_f32_e32 v4, 1.0, v4
	v_rcp_f32_e32 v6, v6
	v_rcp_f32_e32 v2, v2
	v_rcp_f32_e32 v9, v4
	v_add_f32_e32 v4, 1.0, v7
	v_add_f32_e32 v5, 1.0, v5
	v_rcp_f32_e32 v3, v3
	v_rcp_f32_e32 v4, v4
	v_rcp_f32_e32 v5, v5
	s_mov_b64 s[6:7], 0x58000
	v_lshl_add_u64 v[18:19], v[164:165], 0, s[6:7]
	s_mov_b32 s6, 0x58000
	v_cvt_pk_bf16_f32 v2, v6, v2
	v_add_co_u32_e32 v6, vcc, s6, v164
	v_cvt_pk_bf16_f32 v3, v3, v4
	v_cvt_pk_bf16_f32 v4, v20, v8
	v_cvt_pk_bf16_f32 v5, v9, v5
	v_addc_co_u32_e32 v7, vcc, 0, v165, vcc
	global_store_dwordx4 v[6:7], v[2:5], off
	v_pk_fma_f32 v[8:9], v[12:13], v[162:163], v[108:109] op_sel_hi:[1,0,1]
	v_pk_fma_f32 v[6:7], v[10:11], v[162:163], v[106:107] op_sel_hi:[1,0,1]
	v_pk_fma_f32 v[2:3], v[16:17], v[162:163], v[112:113] op_sel_hi:[1,0,1]
	s_nop 0
	s_nop 0
	v_exp_f32_e32 v2, v2
	v_exp_f32_e32 v8, v8
	v_pk_fma_f32 v[4:5], v[14:15], v[162:163], v[110:111] op_sel_hi:[1,0,1]
	s_nop 0
	v_add_f32_e32 v2, 1.0, v2
	s_nop 0
	s_nop 0
	s_nop 0
	s_nop 0
	v_rcp_f32_e32 v10, v2
	v_add_f32_e32 v2, 1.0, v8
	v_exp_f32_e32 v3, v3
	v_mov_b32_e32 v8, v9
	v_exp_f32_e32 v4, v4
	v_exp_f32_e32 v6, v6
	v_exp_f32_e32 v5, v5
	v_exp_f32_e32 v7, v7
	v_exp_f32_e32 v8, v8
	v_rcp_f32_e32 v9, v2
	v_add_f32_e32 v2, 1.0, v3
	v_add_f32_e32 v4, 1.0, v4
	v_add_f32_e32 v6, 1.0, v6
	v_add_f32_e32 v5, 1.0, v5
	v_add_f32_e32 v7, 1.0, v7
	v_rcp_f32_e32 v3, v2
	v_add_f32_e32 v2, 1.0, v8
	v_rcp_f32_e32 v4, v4
	v_rcp_f32_e32 v6, v6
	v_rcp_f32_e32 v5, v5
	v_rcp_f32_e32 v7, v7
	v_rcp_f32_e32 v8, v2
	v_cvt_pk_bf16_f32 v3, v10, v3
	v_cvt_pk_bf16_f32 v2, v4, v5
	v_cvt_pk_bf16_f32 v4, v6, v7
	v_cvt_pk_bf16_f32 v5, v9, v8
	s_and_b64 vcc, exec, s[4:5]
	s_mov_b64 s[4:5], -1
	global_store_dwordx4 v[18:19], v[2:5], off offset:256
	s_cbranch_vccnz .LBB0_1163
	s_andn2_b64 vcc, exec, s[2:3]
	s_cbranch_vccnz .LBB0_1162
	s_barrier
	s_branch .LBB0_1162
